# p13 overlapped weight copies paced with s_sleep 64 per item so they take less of the CU load path from the scan
# speedup vs baseline: 1.0118x; 1.0118x over previous
.LBB0_1365:
	s_sleep 64
	s_waitcnt vmcnt(0)
	ds_write_b32 v71, v2
	ds_write_b32 v72, v3
	ds_write_b32 v73, v4
	ds_write_b32 v74, v5
	ds_write_b32 v76, v6
	ds_write_b32 v77, v7
	ds_write_b32 v78, v8
	ds_write_b32 v79, v9
	ds_write_b32 v81, v26
	ds_write_b32 v82, v27
	ds_write_b32 v83, v28
	ds_write_b32 v84, v29
	ds_write_b32 v86, v30
	ds_write_b32 v87, v31
	ds_write_b32 v88, v32
	ds_write_b32 v89, v33
	ds_write_b32 v91, v34
	ds_write_b32 v92, v35
	ds_write_b32 v93, v36
	ds_write_b32 v94, v37
	ds_write_b32 v96, v38
	ds_write_b32 v97, v39
	ds_write_b32 v98, v40
	ds_write_b32 v99, v41
	ds_write_b32 v101, v42
	ds_write_b32 v102, v43
	ds_write_b32 v103, v44
	ds_write_b32 v104, v45
	ds_write_b32 v106, v46
	ds_write_b32 v107, v47
	ds_write_b32 v108, v48
	ds_write_b32 v109, v49
	ds_write_b32 v111, v50
	ds_write_b32 v112, v51
	ds_write_b32 v113, v52
	ds_write_b32 v114, v53
	ds_write_b32 v116, v54
	ds_write_b32 v117, v55
	ds_write_b32 v118, v56
	ds_write_b32 v119, v57
	ds_write_b32 v121, v58
	ds_write_b32 v122, v59
	ds_write_b32 v123, v60
	ds_write_b32 v124, v61
	ds_write_b32 v126, v62
	ds_write_b32 v127, v63
	ds_write_b32 v128, v64
	ds_write_b32 v129, v65
	ds_write_b32 v131, v22
	ds_write_b32 v132, v23
	ds_write_b32 v133, v24
	ds_write_b32 v134, v25
	ds_write_b32 v136, v18
	ds_write_b32 v137, v19
	ds_write_b32 v138, v20
	ds_write_b32 v139, v21
	ds_write_b32 v141, v14
	ds_write_b32 v142, v15
	ds_write_b32 v143, v16
	ds_write_b32 v144, v17
	ds_write_b32 v146, v10
	ds_write_b32 v147, v11
	ds_write_b32 v148, v12
	ds_write_b32 v149, v13
	s_waitcnt lgkmcnt(0)
	s_add_i32 s26, s19, 0xfffffe00
	s_cmpk_gt_i32 s26, 0xfff
	s_cbranch_scc1 .LBB0_1364
	s_ashr_i32 s0, s19, 31
	s_lshr_b32 s0, s0, 23
	s_add_i32 s0, s19, s0
	s_ashr_i32 s0, s0, 9
	s_add_i32 s10, s0, 16
	s_ashr_i32 s11, s10, 31
	s_mov_b64 s[16:17], 0x32400000
	s_cmpk_lt_i32 s26, 0xfa01
	s_mov_b64 s[14:15], s[10:11]
	s_cbranch_scc1 .LBB0_1363
	s_cmp_gt_u32 s10, 21
	s_cbranch_scc0 .LBB0_1369
	s_add_i32 s14, s0, -6
	s_mov_b32 s15, s1
	s_mov_b64 s[16:17], 0x36400000
	s_cbranch_execnz .LBB0_1363
	s_branch .LBB0_1370

.LBB0_3683:
	s_sleep 64
	s_waitcnt vmcnt(0)
	ds_write_b32 v71, v2
	ds_write_b32 v72, v3
	ds_write_b32 v73, v4
	ds_write_b32 v74, v5
	ds_write_b32 v76, v6
	ds_write_b32 v77, v7
	ds_write_b32 v78, v8
	ds_write_b32 v79, v9
	ds_write_b32 v81, v26
	ds_write_b32 v82, v27
	ds_write_b32 v83, v28
	ds_write_b32 v84, v29
	ds_write_b32 v86, v30
	ds_write_b32 v87, v31
	ds_write_b32 v88, v32
	ds_write_b32 v89, v33
	ds_write_b32 v91, v34
	ds_write_b32 v92, v35
	ds_write_b32 v93, v36
	ds_write_b32 v94, v37
	ds_write_b32 v96, v38
	ds_write_b32 v97, v39
	ds_write_b32 v98, v40
	ds_write_b32 v99, v41
	ds_write_b32 v101, v42
	ds_write_b32 v102, v43
	ds_write_b32 v103, v44
	ds_write_b32 v104, v45
	ds_write_b32 v106, v46
	ds_write_b32 v107, v47
	ds_write_b32 v108, v48
	ds_write_b32 v109, v49
	ds_write_b32 v111, v50
	ds_write_b32 v112, v51
	ds_write_b32 v113, v52
	ds_write_b32 v114, v53
	ds_write_b32 v116, v54
	ds_write_b32 v117, v55
	ds_write_b32 v118, v56
	ds_write_b32 v119, v57
	ds_write_b32 v121, v58
	ds_write_b32 v122, v59
	ds_write_b32 v123, v60
	ds_write_b32 v124, v61
	ds_write_b32 v126, v62
	ds_write_b32 v127, v63
	ds_write_b32 v128, v64
	ds_write_b32 v129, v65
	ds_write_b32 v131, v22
	ds_write_b32 v132, v23
	ds_write_b32 v133, v24
	ds_write_b32 v134, v25
	ds_write_b32 v136, v18
	ds_write_b32 v137, v19
	ds_write_b32 v138, v20
	ds_write_b32 v139, v21
	ds_write_b32 v141, v14
	ds_write_b32 v142, v15
	ds_write_b32 v143, v16
	ds_write_b32 v144, v17
	ds_write_b32 v146, v10
	ds_write_b32 v147, v11
	ds_write_b32 v148, v12
	ds_write_b32 v149, v13
	s_waitcnt lgkmcnt(0)
	s_add_i32 s26, s22, 0xfffffe00
	s_cmpk_gt_i32 s26, 0xfff
	s_cbranch_scc1 .LBB0_3682
	s_ashr_i32 s0, s22, 31
	s_lshr_b32 s0, s0, 23
	s_add_i32 s0, s22, s0
	s_ashr_i32 s0, s0, 9
	s_add_i32 s14, s0, 16
	s_ashr_i32 s15, s14, 31
	s_mov_b64 s[20:21], 0x32400000
	s_cmpk_lt_i32 s26, 0xfa01
	s_mov_b64 s[18:19], s[14:15]
	s_cbranch_scc1 .LBB0_3681
	s_cmp_gt_u32 s14, 21
	s_cbranch_scc0 .LBB0_3687
	s_add_i32 s18, s0, -6
	s_mov_b32 s19, s1
	s_mov_b64 s[20:21], 0x36400000
	s_cbranch_execnz .LBB0_3681
	s_branch .LBB0_3688
